# tile rasterisation: group height 4 for MoE GU/DN and the even in-projection, 2 for the odd in-projection (each A tile shared by all its N tiles concurrently on one XCD)
# speedup vs baseline: 1.0035x; 1.0035x over previous
.LBB0_189:
	s_cmp_eq_u32 s54, 15
	v_writelane_b32 v252, s35, 12
	s_cselect_b64 s[0:1], -1, 0
	v_writelane_b32 v252, s0, 13
	s_cmp_eq_u32 s54, 14
	v_mov_b32_e32 v228, 1
	v_writelane_b32 v252, s1, 14
	s_cselect_b64 s[0:1], -1, 0
	v_writelane_b32 v252, s0, 15
	s_cmp_eq_u32 s54, 13
	v_mov_b32_e32 v222, 0x7f7f7f7f
	v_writelane_b32 v252, s1, 16
	s_cselect_b64 s[0:1], -1, 0
	v_writelane_b32 v252, s0, 17
	s_cmp_eq_u32 s54, 12
	v_mov_b32_e32 v186, 0x358637bd
	v_writelane_b32 v252, s1, 18
	s_cselect_b64 s[0:1], -1, 0
	v_writelane_b32 v252, s0, 19
	s_cmp_eq_u32 s54, 11
	v_mov_b32_e32 v224, 0x42800000
	v_writelane_b32 v252, s1, 20
	s_cselect_b64 s[0:1], -1, 0
	v_writelane_b32 v252, s0, 21
	s_cmp_eq_u32 s54, 10
	v_not_b32_e32 v225, 63
	v_writelane_b32 v252, s1, 22
	s_cselect_b64 s[0:1], -1, 0
	v_writelane_b32 v252, s0, 23
	s_cmp_eq_u32 s54, 9
	v_mov_b64_e32 v[230:231], 0x3ff
	v_writelane_b32 v252, s1, 24
	s_cselect_b64 s[0:1], -1, 0
	v_writelane_b32 v252, s0, 25
	s_cmp_eq_u32 s54, 8
	v_mov_b64_e32 v[248:249], 0x400
	v_writelane_b32 v252, s1, 26
	s_cselect_b64 s[0:1], -1, 0
	v_writelane_b32 v252, s0, 27
	s_cmp_eq_u32 s54, 7
	v_mov_b64_e32 v[250:251], 0x1ff
	v_writelane_b32 v252, s1, 28
	s_cselect_b64 s[0:1], -1, 0
	v_writelane_b32 v252, s0, 29
	s_cmp_eq_u32 s54, 6
	v_mov_b32_e32 v187, 0x4ba00000
	v_writelane_b32 v252, s1, 30
	s_cselect_b64 s[0:1], -1, 0
	v_writelane_b32 v252, s0, 31
	s_cmp_eq_u32 s54, 5
	v_mov_b32_e32 v223, 0x4b200000
	v_writelane_b32 v252, s1, 32
	s_cselect_b64 s[0:1], -1, 0
	v_writelane_b32 v252, s0, 33
	s_cmp_eq_u32 s54, 4
	v_mov_b32_e32 v229, 0xf149f2ca
	v_writelane_b32 v252, s1, 34
	s_cselect_b64 s[0:1], -1, 0
	v_writelane_b32 v252, s0, 35
	s_cmp_eq_u32 s54, 3
	s_mov_b32 s37, 0xefa18f08
	v_writelane_b32 v252, s1, 36
	s_cselect_b64 s[0:1], -1, 0
	v_writelane_b32 v252, s0, 37
	s_cmp_eq_u32 s54, 2
	s_mov_b32 s23, 0xc0e00000
	v_writelane_b32 v252, s1, 38
	s_cselect_b64 s[0:1], -1, 0
	v_writelane_b32 v252, s0, 39
	s_cmp_eq_u32 s54, 1
	s_mov_b32 s36, 0x3fb8aa3b
	v_writelane_b32 v252, s1, 40
	s_cselect_b64 s[0:1], -1, 0
	v_writelane_b32 v252, s0, 41
	s_cmp_eq_u32 s54, 0
	s_nop 0
	v_writelane_b32 v252, s1, 42
	s_cselect_b64 s[0:1], -1, 0
	v_writelane_b32 v252, s0, 43
	s_nop 1
	v_writelane_b32 v252, s1, 44
	s_lshl_b32 s0, s54, 6
	s_cmpk_lt_i32 s88, 0x100
	v_writelane_b32 v252, s0, 45
	s_cselect_b64 s[0:1], -1, 0
	v_writelane_b32 v252, s0, 46
	s_cmpk_lt_i32 s88, 0x800
	s_nop 0
	v_writelane_b32 v252, s1, 47
	s_cselect_b64 s[0:1], -1, 0
	v_writelane_b32 v252, s0, 48
	s_nop 1
	v_writelane_b32 v252, s1, 49
	s_ashr_i32 s0, s88, 31
	v_writelane_b32 v252, s0, 50
	s_lshr_b32 s0, s0, 29
	s_add_i32 s0, s88, s0
	v_readlane_b32 s1, v252, 4
	s_ashr_i32 s21, s0, 3
	s_and_b32 s0, s0, -8
	s_lshr_b32 s3, s1, 8
	s_sub_i32 s22, s88, s0
	v_writelane_b32 v252, s3, 51
	s_bfe_u32 s1, s1, 0x20006
	s_lshl_b32 s0, s22, 8
	v_writelane_b32 v252, s1, 52
	s_ashr_i32 s1, s2, 31
	s_cmpk_lt_i32 s88, 0x400
	v_writelane_b32 v252, s1, 53
	s_waitcnt lgkmcnt(0)
	s_cselect_b64 s[4:5], -1, 0
	v_writelane_b32 v252, s4, 54
	s_max_i32 s1, s2, 2
	s_and_b32 s6, s88, 1
	v_writelane_b32 v252, s5, 55
	s_lshr_b32 s4, s1, 1
	v_readlane_b32 s1, v252, 11
	s_and_b32 s1, s1, -16
	s_or_b32 s5, s1, s6
	v_writelane_b32 v252, s5, 56
	s_lshl_b32 s3, s22, 7
	v_writelane_b32 v252, s4, 57
	s_min_i32 s4, s4, 0x80
	s_cmp_gt_i32 s4, s88
	s_cselect_b64 s[4:5], -1, 0
	v_writelane_b32 v252, s4, 58
	s_nop 1
	v_writelane_b32 v252, s5, 59
	s_ashr_i32 s4, s1, 1
	s_ashr_i32 s5, s4, 31
	s_lshl_b64 s[8:9], s[4:5], 19
	v_writelane_b32 v252, s8, 60
	s_lshl_b64 s[4:5], s[4:5], 17
	s_lshl_b32 s1, s6, 17
	v_writelane_b32 v252, s9, 61
	v_writelane_b32 v252, s4, 62
	s_nop 1
	v_writelane_b32 v252, s5, 63
	s_lshr_b32 s4, s2, 31
	s_add_i32 s4, s2, s4
	s_ashr_i32 s4, s4, 1
	s_cmp_gt_i32 s2, 1
	s_cselect_b32 s4, s4, 1
	s_sub_i32 s8, s2, s4
	s_sub_i32 s9, s88, s4
	s_cmp_ge_i32 s88, s4
	s_cselect_b64 s[4:5], -1, 0
	s_and_b64 s[6:7], s[4:5], exec
	s_cselect_b32 s10, s8, 1
	s_cselect_b32 s11, s9, 0
	s_cmp_lt_i32 s2, 2
	s_cselect_b64 s[6:7], -1, 0
	s_and_b64 s[8:9], s[6:7], exec
	s_cselect_b32 s8, 1, s10
	s_cselect_b32 s9, 0, s11
	s_or_b64 s[4:5], s[6:7], s[4:5]
	s_and_b64 s[4:5], s[4:5], exec
	s_cselect_b32 s24, 0x200, 0
	s_cmp_lt_i32 s9, s24
	s_cselect_b64 s[4:5], -1, 0
	v_writelane_b32 v253, s4, 0
	s_lshr_b32 s16, s24, 3
	s_or_b32 s17, s16, 1
	v_writelane_b32 v253, s5, 1
	s_ashr_i32 s4, s9, 31
	v_writelane_b32 v253, s4, 2
	s_lshr_b32 s4, s4, 29
	s_add_i32 s4, s9, s4
	s_ashr_i32 s6, s4, 3
	s_and_b32 s4, s4, -8
	v_writelane_b32 v253, s9, 3
	s_sub_i32 s7, s9, s4
	s_ashr_i32 s4, s8, 31
	s_lshl_b32 s34, s2, 4
	v_writelane_b32 v253, s8, 4
	s_cmpk_lt_i32 s88, 0x200
	v_writelane_b32 v253, s4, 5
	s_cselect_b64 s[4:5], -1, 0
	v_writelane_b32 v253, s4, 6
	s_mul_i32 s10, s22, 0x41
	s_mul_i32 s11, s22, 5
	v_writelane_b32 v253, s5, 7
	s_lshl_b32 s4, s22, 6
	s_cmpk_lt_i32 s88, 0x180
	s_cselect_b64 s[8:9], -1, 0
	v_writelane_b32 v253, s8, 8
	s_cmp_lt_i32 s88, 32
	s_nop 0
	v_writelane_b32 v253, s9, 9
	s_cselect_b64 s[8:9], -1, 0
	v_writelane_b32 v253, s8, 10
	s_lshl_b32 s5, s22, 2
	s_nop 0
	v_writelane_b32 v253, s9, 11
	s_lshl_b32 s8, s88, 9
	v_writelane_b32 v253, s8, 12
	s_lshl_b32 s8, s2, 9
	v_writelane_b32 v253, s8, 13
	s_cmp_lt_i32 s22, 0
	s_mul_i32 s8, s22, 0x101
	s_mul_i32 s9, s22, 0x81
	s_cselect_b32 s0, s8, s0
	s_cselect_b32 s8, s9, s3
	s_cselect_b32 s9, s10, s4
	s_cselect_b32 s10, 49, 48
	s_cselect_b32 s3, s11, s5
	s_add_i32 s0, s0, s21
	s_ashr_i32 s4, s0, 31
	s_lshr_b32 s4, s4, 25
	s_add_i32 s4, s0, s4
	s_ashr_i32 s5, s0, 5
	s_and_b32 s4, s0, 31
	s_and_b32 s11, s4, 1
	s_lshr_b32 s12, s4, 1
	s_nop 0
	s_nop 0
	s_nop 0
	s_nop 0
	s_nop 0
	s_lshl_b32 s5, s5, 1
	s_nop 0
	s_nop 0
	s_add_i32 s8, s8, s21
	s_add_i32 s26, s5, s11
	s_mov_b32 s4, s12
	s_ashr_i32 s11, s8, 31
	v_writelane_b32 v253, s4, 14
	s_lshr_b32 s4, s11, 22
	s_add_i32 s4, s8, s4
	s_ashr_i32 s5, s4, 10
	s_and_b32 s4, s4, 0xfc00
	s_sub_i32 s4, s8, s4
	s_mov_b32 s0, s12
	s_sext_i32_i16 s12, s4
	s_bfe_u32 s12, s12, 0x3001c
	s_add_i32 s12, s4, s12
	s_sext_i32_i16 s13, s12
	s_and_b32 s12, s12, 0xfff8
	s_sub_i32 s12, s4, s12
	s_lshl_b32 s5, s5, 3
	s_sext_i32_i16 s12, s12
	s_lshr_b32 s4, s13, 3
	s_add_i32 s12, s5, s12
	s_ashr_i32 s5, s13, 3
	v_writelane_b32 v253, s5, 15
	s_bfe_i64 s[4:5], s[4:5], 0x100000
	s_lshl_b64 s[4:5], s[4:5], 18
	v_writelane_b32 v253, s4, 16
	s_ashr_i32 s13, s12, 31
	s_mul_i32 s10, s22, s10
	v_writelane_b32 v253, s5, 17
	s_mov_b32 s4, s12
	v_writelane_b32 v253, s4, 18
	s_nop 1
	v_writelane_b32 v253, s5, 19
	s_lshl_b64 s[4:5], s[12:13], 18
	v_writelane_b32 v253, s4, 20
	s_cmp_lt_i32 s7, 0
	s_cselect_b32 s12, s17, s16
	v_writelane_b32 v253, s5, 21
	s_lshr_b32 s4, s11, 28
	s_add_i32 s4, s8, s4
	s_and_b32 s5, s4, 0xfff0
	s_sub_i32 s5, s8, s5
	s_bfe_i32 s13, s5, 0x80000
	s_bfe_u32 s13, s13, 0x3000c
	s_mul_i32 s7, s12, s7
	s_add_i32 s13, s5, s13
	s_add_i32 s6, s7, s6
	s_add_i32 s7, s9, s21
	v_writelane_b32 v253, s16, 22
	s_and_b32 s16, s13, 0xf8
	s_ashr_i32 s9, s7, 31
	s_sub_i32 s16, s5, s16
	s_ashr_i32 s4, s4, 4
	s_lshr_b32 s9, s9, 27
	s_lshl_b32 s4, s4, 3
	s_sext_i32_i8 s5, s16
	s_add_i32 s9, s7, s9
	s_add_i32 s28, s4, s5
	s_and_b32 s12, s9, 0xffe0
	s_ashr_i32 s4, s28, 5
	s_sub_i32 s7, s7, s12
	s_ashr_i32 s5, s4, 31
	s_lshl_b32 s16, s16, 10
	s_bfe_i32 s12, s7, 0x80000
	s_and_b32 s16, s16, 0x1c00
	s_lshl_b64 s[4:5], s[4:5], 13
	s_bfe_u32 s12, s12, 0x3000c
	s_or_b32 s4, s4, s16
	s_bfe_u32 s16, s28, 0x20003
	s_add_i32 s12, s7, s12
	s_lshr_b32 s11, s11, 26
	s_or_b32 s4, s4, s16
	s_and_b32 s16, s12, 0xf8
	s_add_i32 s11, s8, s11
	s_sub_i32 s7, s7, s16
	s_and_b32 s16, s11, 0xffe0
	s_sub_i32 s8, s8, s16
	s_bfe_i32 s16, s8, 0x80000
	s_bfe_u32 s16, s16, 0x3000c
	s_add_i32 s16, s8, s16
	v_writelane_b32 v253, s17, 23
	s_and_b32 s17, s16, 0xfc
	s_add_i32 s10, s10, s21
	s_sub_i32 s8, s8, s17
	s_ashr_i32 s17, s10, 31
	s_lshr_b32 s17, s17, 22
	s_add_i32 s17, s10, s17
	s_and_b32 s18, s17, 0xfffffc00
	s_sub_i32 s10, s10, s18
	s_ashr_i32 s18, s6, 31
	s_lshr_b32 s18, s18, 29
	s_add_i32 s18, s6, s18
	s_and_b32 s18, s18, -8
	s_sub_i32 s20, s6, s18
	s_bfe_i32 s6, s13, 0x80000
	s_lshl_b64 s[4:5], s[4:5], 10
	s_sext_i32_i16 s6, s6
	v_writelane_b32 v253, s4, 24
	s_sext_i32_i8 s8, s8
	s_ashr_i32 s29, s28, 31
	v_writelane_b32 v253, s5, 25
	s_ashr_i32 s4, s6, 3
	v_writelane_b32 v253, s4, 26
	s_lshr_b32 s4, s6, 3
	s_bfe_i64 s[4:5], s[4:5], 0x100000
	s_lshl_b64 s[4:5], s[4:5], 18
	v_writelane_b32 v253, s4, 27
	s_sext_i32_i8 s6, s7
	s_bfe_i32 s7, s16, 0x80000
	v_writelane_b32 v253, s5, 28
	s_ashr_i32 s4, s9, 5
	s_bfe_i32 s5, s12, 0x80000
	s_lshl_b32 s4, s4, 3
	s_sext_i32_i16 s5, s5
	s_add_i32 s30, s4, s6
	s_ashr_i32 s4, s5, 3
	v_writelane_b32 v253, s4, 29
	s_ashr_i32 s6, s11, 5
	s_sext_i32_i16 s7, s7
	s_lshl_b32 s6, s6, 2
	v_writelane_b32 v253, s21, 30
	s_add_i32 s9, s3, s21
	s_ashr_i32 s3, s7, 2
	s_add_i32 s16, s6, s8
	v_writelane_b32 v253, s3, 31
	s_mov_b32 s8, s28
	v_writelane_b32 v253, s8, 32
	s_lshl_b64 s[28:29], s[28:29], 19
	s_ashr_i32 s31, s30, 31
	v_writelane_b32 v253, s9, 33
	s_ashr_i32 s6, s17, 10
	v_writelane_b32 v253, s28, 34
	s_lshr_b32 s4, s5, 3
	s_lshl_b32 s11, s6, 3
	v_writelane_b32 v253, s29, 35
	s_lshl_b64 s[28:29], s[30:31], 19
	s_sub_i32 s19, s24, s18
	s_bfe_i64 s[4:5], s[4:5], 0x100000
	s_sub_i32 s6, 3, s11
	v_writelane_b32 v253, s28, 36
	s_min_i32 s19, s19, 8
	s_min_u32 s12, s6, 8
	s_lshr_b32 s6, s7, 2
	v_writelane_b32 v253, s29, 37
	s_lshl_b64 s[28:29], s[4:5], 19
	v_writelane_b32 v253, s28, 38
	s_cmp_lt_u32 s9, 16
	v_cvt_f32_i32_e32 v1, s20
	v_writelane_b32 v253, s29, 39
	s_cselect_b64 s[28:29], -1, 0
	v_writelane_b32 v253, s28, 40
	s_ashr_i32 s8, s9, 4
	s_lshl_b32 s3, s9, 18
	v_writelane_b32 v253, s29, 41
	v_writelane_b32 v253, s9, 42
	s_ashr_i32 s9, s8, 31
	s_lshl_b64 s[8:9], s[8:9], 20
	v_writelane_b32 v253, s8, 43
	s_ashr_i32 s27, s26, 31
	s_ashr_i32 s17, s16, 31
	v_writelane_b32 v253, s9, 44
	s_lshl_b64 s[8:9], s[4:5], 18
	v_writelane_b32 v253, s8, 45
	s_lshl_b64 s[4:5], s[4:5], 17
	s_and_b32 s3, s3, 0x3c0000
	v_writelane_b32 v253, s9, 46
	v_writelane_b32 v253, s4, 47
	s_mov_b32 s29, 0
	s_mov_b32 s25, s29
	v_writelane_b32 v253, s5, 48
	s_bfe_i64 s[4:5], s[0:1], 0x100000
	s_lshl_b64 s[4:5], s[4:5], 18
	v_writelane_b32 v253, s4, 49
	s_sext_i32_i16 s0, s19
	v_cvt_f32_i32_e32 v0, s0
	v_writelane_b32 v253, s5, 50
	s_bfe_i64 s[4:5], s[6:7], 0x100000
	s_lshl_b64 s[4:5], s[4:5], 19
	v_writelane_b32 v253, s4, 51
	v_rcp_iflag_f32_e32 v2, v0
	s_mov_b32 s19, 0xf149f2ca
	v_writelane_b32 v253, s5, 52
	s_xor_b32 s4, s20, s0
	s_ashr_i32 s4, s4, 30
	s_or_b32 s6, s4, 1
	v_writelane_b32 v253, s22, 53
	s_lshr_b32 s4, s22, 31
	v_writelane_b32 v253, s4, 54
	s_lshl_b64 s[4:5], s[30:31], 18
	v_writelane_b32 v253, s4, 55
	v_mul_f32_e32 v2, v1, v2
	v_trunc_f32_e32 v2, v2
	v_writelane_b32 v253, s5, 56
	s_mov_b32 s4, s30
	v_writelane_b32 v253, s4, 57
	v_fma_f32 v1, -v2, v0, v1
	s_mov_b32 s22, 0x3d000000
	v_writelane_b32 v253, s5, 58
	s_lshl_b64 s[4:5], s[30:31], 17
	v_writelane_b32 v253, s4, 59
	s_mov_b32 s30, 0xc01d265f
	s_nop 0
	v_writelane_b32 v253, s5, 60
	s_mov_b32 s4, s26
	v_writelane_b32 v253, s4, 61
	s_nop 1
	v_writelane_b32 v253, s5, 62
	s_lshl_b64 s[4:5], s[26:27], 18
	v_writelane_b32 v253, s4, 63
	s_mov_b32 s26, 0x3b800000
	s_nop 0
	v_writelane_b32 v254, s5, 0
	s_mov_b32 s4, s16
	v_writelane_b32 v254, s4, 1
	s_nop 1
	v_writelane_b32 v254, s5, 2
	s_lshl_b64 s[4:5], s[16:17], 19
	v_writelane_b32 v254, s4, 3
	s_mov_b32 s17, 0x800000
	s_mov_b32 s16, 0x3b000000
	v_writelane_b32 v254, s5, 4
	v_cmp_ge_f32_e64 s[4:5], |v1|, |v0|
	v_cvt_i32_f32_e32 v0, v2
	s_and_b64 s[4:5], s[4:5], exec
	s_cselect_b32 s4, s6, 0
	v_cvt_f32_ubyte0_e32 v1, s12
	v_readfirstlane_b32 s5, v0
	s_add_i32 s4, s5, s4
	s_mul_i32 s4, s4, s0
	s_sub_i32 s0, s20, s4
	s_sext_i32_i16 s4, s0
	s_add_i32 s9, s18, s4
	s_ashr_i32 s4, s9, 5
	s_ashr_i32 s5, s4, 31
	s_lshl_b32 s6, s0, 10
	s_and_b32 s8, s6, 0x1c00
	s_lshl_b64 s[6:7], s[4:5], 13
	s_or_b32 s6, s6, s8
	s_bfe_u32 s8, s9, 0x20003
	s_or_b32 s6, s6, s8
	v_cvt_f32_i32_e32 v0, s10
	v_rcp_iflag_f32_e32 v2, v1
	s_lshl_b64 s[6:7], s[6:7], 10
	v_writelane_b32 v254, s6, 5
	s_lshl_b64 s[4:5], s[4:5], 22
	v_mul_f32_e32 v2, v0, v2
	v_writelane_b32 v254, s7, 6
	v_writelane_b32 v254, s4, 7
	v_trunc_f32_e32 v2, v2
	v_fma_f32 v0, -v2, v1, v0
	v_writelane_b32 v254, s5, 8
	s_lshl_b32 s4, s9, 5
	s_and_b32 s6, s4, 0x300
	s_ashr_i32 s4, s10, 30
	s_or_b32 s7, s4, 1
	v_cmp_ge_f32_e64 s[4:5], |v0|, v1
	v_cvt_i32_f32_e32 v0, v2
	s_lshl_b32 s0, s0, 18
	s_and_b32 s0, s0, 0x1c0000
	s_and_b64 s[4:5], s[4:5], exec
	s_cselect_b32 s4, s7, 0
	v_readfirstlane_b32 s5, v0
	s_add_i32 s4, s5, s4
	s_mul_i32 s5, s4, s12
	s_sub_i32 s5, s10, s5
	s_sext_i32_i16 s5, s5
	v_writelane_b32 v254, s9, 9
	s_add_i32 s5, s11, s5
	v_writelane_b32 v254, s5, 10
	s_abs_i32 s5, s2
	v_cvt_f32_u32_e32 v0, s5
	v_writelane_b32 v254, s5, 11
	s_sub_i32 s5, 0, s5
	s_sext_i32_i16 s4, s4
	v_rcp_iflag_f32_e32 v0, v0
	s_lshl_b32 s1, s1, 1
	s_lshl_b32 s0, s0, 1
	s_ashr_i32 s35, s34, 31
	v_mul_f32_e32 v0, 0x4f7ffffe, v0
	v_cvt_u32_f32_e32 v0, v0
	v_mov_b32_e32 v1, 0
	s_add_i32 s31, 0, 0x23600
	s_mov_b32 s18, 0xbd38aa3b
	v_readfirstlane_b32 s7, v0
	s_mul_i32 s5, s5, s7
	s_mul_hi_u32 s5, s7, s5
	s_add_i32 s5, s7, s5
	v_writelane_b32 v254, s5, 12
	v_writelane_b32 v254, s24, 13
	s_nop 1
	v_writelane_b32 v254, s25, 14
	v_writelane_b32 v254, s4, 15
	v_writelane_b32 v254, s1, 16
	v_writelane_b32 v254, s0, 17
	s_lshl_b32 s0, s6, 1
	v_writelane_b32 v254, s0, 18
	s_lshl_b32 s0, s3, 1
	v_writelane_b32 v254, s0, 19
	s_lshl_b32 s0, s88, 7
	v_writelane_b32 v254, s0, 20
	s_lshl_b32 s0, s2, 7
	v_writelane_b32 v254, s0, 21
	s_lshl_b32 s0, s88, 5
	v_writelane_b32 v254, s0, 22
	s_lshl_b32 s0, s2, 5
	v_writelane_b32 v254, s0, 23
	s_add_i32 s0, 0, 0x22000
	v_writelane_b32 v254, s0, 24
	s_add_i32 s0, 0, 0x22004
	v_writelane_b32 v254, s0, 25
	s_add_i32 s0, 0, 0x22d10
	v_writelane_b32 v254, s0, 26
	s_add_i32 s0, 0, 0x22d20
	v_writelane_b32 v254, s0, 27
	s_add_i32 s0, 0, 0x22d30
	v_writelane_b32 v254, s0, 28
	s_add_i32 s0, 0, 0x22d40
	v_writelane_b32 v254, s0, 29
	s_add_i32 s0, 0, 0x22d50
	v_writelane_b32 v254, s0, 30
	s_add_i32 s0, 0, 0x22d60
	v_writelane_b32 v254, s0, 31
	s_add_i32 s0, 0, 0x22d70
	v_writelane_b32 v254, s0, 32
	s_add_i32 s0, 0, 0x22500
	v_writelane_b32 v254, s0, 33
	s_add_i32 s0, 0, 0x23500
	v_writelane_b32 v254, s0, 34
	s_add_i32 s0, 0, 0x22d80
	v_writelane_b32 v254, s0, 35
	s_add_i32 s0, 0, 0x22d90
	v_writelane_b32 v254, s0, 36
	s_add_i32 s0, 0, 0x22da0
	v_writelane_b32 v254, s0, 37
	s_add_i32 s0, 0, 0x22db0
	v_writelane_b32 v254, s0, 38
	s_add_i32 s0, 0, 0x22dc0
	v_writelane_b32 v254, s0, 39
	s_add_i32 s0, 0, 0x22dd0
	v_writelane_b32 v254, s0, 40
	s_add_i32 s0, 0, 0x22de0
	v_writelane_b32 v254, s0, 41
	s_add_i32 s0, 0, 0x22df0
	v_writelane_b32 v254, s0, 42
	s_add_i32 s0, 0, 0x22100
	v_writelane_b32 v254, s0, 43
	s_add_i32 s0, 0, 0x23510
	v_writelane_b32 v254, s0, 44
	s_add_i32 s0, 0, 0x23610
	v_writelane_b32 v254, s0, 45
	s_add_i32 s0, 0, 0x23520
	v_writelane_b32 v254, s0, 46
	s_add_i32 s0, 0, 0x23620
	v_writelane_b32 v254, s0, 47
	s_add_i32 s0, 0, 0x23530
	v_writelane_b32 v254, s0, 48
	s_add_i32 s0, 0, 0x23630
	v_writelane_b32 v254, s0, 49
	s_add_i32 s0, 0, 0x23540
	v_writelane_b32 v254, s0, 50
	s_add_i32 s0, 0, 0x23640
	v_writelane_b32 v254, s0, 51
	s_add_i32 s0, 0, 0x23550
	v_writelane_b32 v254, s0, 52
	s_add_i32 s0, 0, 0x23650
	v_writelane_b32 v254, s0, 53
	s_add_i32 s0, 0, 0x23560
	v_writelane_b32 v254, s0, 54
	s_add_i32 s0, 0, 0x23660
	v_writelane_b32 v254, s0, 55
	s_add_i32 s0, 0, 0x23570
	v_writelane_b32 v254, s0, 56
	s_add_i32 s0, 0, 0x23670
	v_writelane_b32 v254, s0, 57
	s_add_i32 s0, 0, 0x23680
	v_writelane_b32 v254, s0, 58
	s_lshl_b64 s[4:5], s[34:35], 11
	v_writelane_b32 v254, s4, 59
	s_movk_i32 s1, 0x200
	s_add_i32 s3, 0, 0x24a00
	v_writelane_b32 v254, s5, 60
	s_lshl_b64 s[4:5], s[34:35], 10
	v_writelane_b32 v254, s4, 61
	s_mov_b64 s[24:25], 0x80
	s_mov_b32 s0, 0x3e000000
	v_writelane_b32 v254, s5, 62
	s_mov_b32 s4, s88
	v_writelane_b32 v254, s4, 63
	s_mov_b32 s6, s29
	s_nop 0
	v_writelane_b32 v255, s5, 0
	v_writelane_b32 v255, s34, 1
	s_nop 1
	v_writelane_b32 v255, s35, 2
	s_branch .LBB0_193

.LBB0_373:
	s_ashr_i32 s12, s28, 3
	s_add_i32 s12, s43, s12
	s_ashr_i32 s13, s12, 31
	s_lshr_b32 s13, s13, 27
	s_add_i32 s13, s12, s13
	s_ashr_i32 s28, s13, 5
	s_lshl_b32 s28, s28, 1
	s_sub_i32 s42, 0x80, s28
	s_min_i32 s43, s42, 2
	s_abs_i32 s42, s43
	v_cvt_f32_u32_e32 v2, s42
	s_sub_i32 s45, 0, s42
	s_and_b32 s13, s13, 0xffffffe0
	s_sub_i32 s12, s12, s13
	v_rcp_iflag_f32_e32 v2, v2
	s_abs_i32 s13, s12
	s_xor_b32 s44, s12, s43
	s_ashr_i32 s44, s44, 31
	v_mul_f32_e32 v2, 0x4f7ffffe, v2
	v_cvt_u32_f32_e32 v2, v2
	s_nop 0
	v_readfirstlane_b32 s47, v2
	s_mul_i32 s45, s45, s47
	s_mul_hi_u32 s45, s47, s45
	s_add_i32 s47, s47, s45
	s_mul_hi_u32 s45, s13, s47
	s_mul_i32 s47, s45, s42
	s_sub_i32 s13, s13, s47
	s_add_i32 s48, s45, 1
	s_sub_i32 s47, s13, s42
	s_cmp_ge_u32 s13, s42
	s_cselect_b32 s45, s48, s45
	s_cselect_b32 s13, s47, s13
	s_add_i32 s47, s45, 1
	s_cmp_ge_u32 s13, s42
	s_cselect_b32 s13, s47, s45
	s_xor_b32 s13, s13, s44
	s_sub_i32 s42, s13, s44
	s_mul_i32 s13, s42, s43
	s_sub_i32 s12, s12, s13
	s_add_i32 s44, s28, s12

.LBB0_971:
	s_ashr_i32 s12, s14, 3
	s_add_i32 s12, s28, s12
	s_ashr_i32 s13, s12, 31
	s_lshr_b32 s13, s13, 27
	s_add_i32 s13, s12, s13
	s_ashr_i32 s14, s13, 5
	s_lshl_b32 s14, s14, 2
	s_sub_i32 s15, 0x80, s14
	s_min_i32 s15, s15, 4
	s_abs_i32 s28, s15
	v_cvt_f32_u32_e32 v0, s28
	s_sub_i32 s35, 0, s28
	s_andn2_b32 s13, s13, 31
	s_sub_i32 s13, s12, s13
	v_rcp_iflag_f32_e32 v0, v0
	s_abs_i32 s12, s13
	s_xor_b32 s34, s13, s15
	s_ashr_i32 s34, s34, 31
	v_mul_f32_e32 v0, 0x4f7ffffe, v0
	v_cvt_u32_f32_e32 v0, v0
	s_nop 0
	v_readfirstlane_b32 s38, v0
	s_mul_i32 s35, s35, s38
	s_mul_hi_u32 s35, s38, s35
	s_add_i32 s38, s38, s35
	s_mul_hi_u32 s35, s12, s38
	s_mul_i32 s38, s35, s28
	s_sub_i32 s12, s12, s38
	s_add_i32 s39, s35, 1
	s_sub_i32 s38, s12, s28
	s_cmp_ge_u32 s12, s28
	s_cselect_b32 s35, s39, s35
	s_cselect_b32 s12, s38, s12
	s_add_i32 s38, s35, 1
	s_cmp_ge_u32 s12, s28
	s_cselect_b32 s12, s38, s35
	s_xor_b32 s12, s12, s34
	s_sub_i32 s12, s12, s34
	s_mul_i32 s15, s12, s15
	s_sub_i32 s13, s13, s15
	s_add_i32 s14, s14, s13

.LBB0_1685:
	v_readlane_b32 s6, v254, 58
	s_nop 1
	v_mov_b32_e32 v0, s6
	ds_read_b32 v0, v0
	v_readlane_b32 s6, v255, 4
	v_readlane_b32 s7, v255, 5
	s_mov_b32 s7, s29
	v_writelane_b32 v255, s6, 4
	s_waitcnt lgkmcnt(0)
	v_lshlrev_b32_e32 v178, 3, v0
	s_waitcnt vmcnt(0)
	v_mbcnt_lo_u32_b32 v6, -1, 0
	v_mbcnt_hi_u32_b32 v6, -1, v6
	v_readfirstlane_b32 s27, v0
	v_or_b32_e32 v0, s33, v6
	v_cmp_ge_i32_e32 vcc, s88, v178
	v_writelane_b32 v255, s7, 5
	v_readfirstlane_b32 s28, v0
	s_cbranch_vccnz .LBB0_1707
	v_lshlrev_b32_e32 v3, 4, v0
	v_add_u32_e32 v2, 0x2000, v3
	v_ashrrev_i32_e32 v4, 31, v2
	v_lshrrev_b32_e32 v4, 22, v4
	v_add_u32_e32 v4, v2, v4
	v_ashrrev_i32_e32 v4, 10, v4
	v_mul_i32_i24_e32 v5, 0x400, v4
	v_sub_u32_e32 v2, v2, v5
	v_lshrrev_b32_e32 v5, 4, v2
	v_bitop3_b32 v5, v5, v2, 32 bitop3:0x6c
	v_ashrrev_i32_e32 v2, 31, v5
	v_lshrrev_b32_e32 v2, 26, v2
	v_add_u32_e32 v7, v5, v2
	v_ashrrev_i32_e32 v8, 6, v7
	v_and_b32_e32 v7, 0xc0, v7
	v_sub_u32_e32 v5, v5, v7
	v_lshlrev_b32_e32 v2, 3, v4
	v_lshlrev_b32_e32 v4, 5, v4
	v_ashrrev_i16_sdwa v5, v228, sext(v5) dst_sel:DWORD dst_unused:UNUSED_PAD src0_sel:DWORD src1_sel:BYTE_0
	v_and_b32_e32 v4, 32, v4
	v_bfe_i32 v5, v5, 0, 16
	v_add_lshl_u32 v7, v4, v5, 1
	v_bfe_i32 v4, v0, 27, 1
	v_lshrrev_b32_e32 v4, 22, v4
	v_add_u32_e32 v4, v3, v4
	v_and_b32_e32 v4, 0xfffffc00, v4
	v_sub_u32_e32 v3, v3, v4
	v_readlane_b32 s6, v255, 4
	v_lshrrev_b32_e32 v4, 4, v3
	s_add_u32 s12, s10, 0x34800000
	v_readlane_b32 s7, v255, 5
	v_bitop3_b32 v3, v4, v3, 32 bitop3:0x6c
	s_addc_u32 s13, s11, 0
	s_lshl_b64 s[6:7], s[6:7], 26
	v_ashrrev_i32_e32 v4, 31, v3
	s_add_u32 s6, s10, s6
	v_lshrrev_b32_e32 v4, 26, v4
	s_addc_u32 s7, s11, s7
	v_and_b32_e32 v2, -16, v2
	v_add_u32_e32 v5, v3, v4
	v_ashrrev_i32_e32 v4, 31, v0
	s_add_u32 s56, s6, 0x4400000
	v_add_u32_e32 v2, v8, v2
	v_lshrrev_b32_e32 v4, 26, v4
	s_addc_u32 s57, s7, 0
	s_load_dwordx2 s[6:7], s[4:5], 0xa8
	v_and_b32_e32 v8, 3, v8
	s_mov_b32 s4, 0x3fffe0
	v_lshrrev_b32_e32 v9, 2, v2
	v_lshlrev_b32_e32 v10, 1, v2
	v_add_u32_e32 v0, v0, v4
	v_and_or_b32 v8, v2, s4, v8
	v_and_b32_e32 v9, 4, v9
	v_and_b32_e32 v10, 24, v10
	v_ashrrev_i32_e32 v0, 6, v0
	v_or3_b32 v8, v8, v9, v10
	v_lshlrev_b32_e32 v4, 3, v0
	v_lshl_add_u32 v180, v8, 10, v7
	v_ashrrev_i32_e32 v8, 6, v5
	v_and_b32_e32 v4, -16, v4
	v_add_u32_e32 v4, v8, v4
	v_and_b32_e32 v8, 3, v8
	s_add_u32 s58, s10, 0x89000000
	v_and_or_b32 v8, v4, s4, v8
	v_readlane_b32 s4, v253, 54
	s_addc_u32 s59, s11, 0
	s_add_i32 s4, s27, s4
	v_readlane_b32 s5, v253, 53
	s_mul_i32 s4, s4, s5
	v_readlane_b32 s5, v253, 30
	s_add_i32 s4, s4, s5
	s_ashr_i32 s5, s4, 31
	s_lshr_b32 s5, s5, 27
	s_add_i32 s5, s4, s5
	s_ashr_i32 s15, s5, 5
	v_and_b32_e32 v5, 0xc0, v5
	s_lshl_b32 s15, s15, 2
	v_sub_u32_e32 v3, v3, v5
	s_sub_i32 s20, s27, s15
	v_lshlrev_b32_e32 v0, 5, v0
	v_ashrrev_i16_sdwa v3, v228, sext(v3) dst_sel:DWORD dst_unused:UNUSED_PAD src0_sel:DWORD src1_sel:BYTE_0
	s_min_i32 s20, s20, 4
	v_and_b32_e32 v0, 32, v0
	v_bfe_i32 v3, v3, 0, 16
	s_abs_i32 s34, s20
	v_add_lshl_u32 v3, v0, v3, 1
	v_cvt_f32_u32_e32 v0, s34
	s_sub_i32 s35, 0, s34
	s_andn2_b32 s5, s5, 31
	s_sub_i32 s4, s4, s5
	v_rcp_iflag_f32_e32 v0, v0
	s_abs_i32 s21, s4
	s_ashr_i32 s8, s28, 6
	s_xor_b32 s5, s4, s20
	v_mul_f32_e32 v0, 0x4f7ffffe, v0
	v_cvt_u32_f32_e32 v0, v0
	s_ashr_i32 s9, s28, 8
	s_lshl_b32 s14, s8, 10
	s_ashr_i32 s5, s5, 31
	v_readfirstlane_b32 s38, v0
	s_mul_i32 s35, s35, s38
	s_mul_hi_u32 s35, s38, s35
	s_add_i32 s38, s38, s35
	s_mul_hi_u32 s35, s21, s38
	s_mul_i32 s38, s35, s34
	s_sub_i32 s21, s21, s38
	s_add_i32 s38, s35, 1
	s_sub_i32 s39, s21, s34
	s_cmp_ge_u32 s21, s34
	s_cselect_b32 s35, s38, s35
	s_cselect_b32 s21, s39, s21
	s_add_i32 s38, s35, 1
	v_mbcnt_lo_u32_b32 v0, -1, 0
	v_mbcnt_hi_u32_b32 v0, -1, v0
	s_cmp_ge_u32 s21, s34
	v_and_b32_e32 v0, 31, v0
	s_cselect_b32 s21, s38, s35
	v_lshl_add_u32 v5, v0, 2, s31
	s_xor_b32 s21, s21, s5
	ds_read_b32 v5, v5 offset:4
	s_sub_i32 s46, s21, s5
	s_mul_i32 s5, s46, s20
	s_sub_i32 s4, s4, s5
	s_add_i32 s48, s15, s4
	v_cmp_ne_u32_e32 vcc, 31, v0
	s_waitcnt lgkmcnt(0)
	v_cmp_ge_i32_e64 s[4:5], s48, v5
	s_and_b64 s[4:5], vcc, s[4:5]
	s_ashr_i32 s47, s46, 31
	v_cndmask_b32_e64 v0, 0, 1, s[4:5]
	v_cmp_ne_u32_e32 vcc, 0, v0
	s_bcnt1_i32_b32 s15, vcc_lo
	s_lshl_b64 s[4:5], s[46:47], 18
	s_add_u32 s20, s56, s4
	s_addc_u32 s21, s57, s5
	s_ashr_i32 s49, s48, 31
	s_lshl_b64 s[4:5], s[48:49], 10
	s_add_u32 s4, s58, s4
	s_addc_u32 s5, s59, s5
	v_ashrrev_i32_e32 v5, 31, v4
	v_lshrrev_b32_e32 v9, 2, v4
	v_lshlrev_b32_e32 v10, 1, v4
	v_lshl_add_u64 v[4:5], v[4:5], 2, s[4:5]
	global_load_dword v0, v[4:5], off
	v_and_b32_e32 v9, 4, v9
	global_load_dword v4, v[4:5], off offset:512
	v_and_b32_e32 v10, 24, v10
	v_or3_b32 v8, v8, v9, v10
	v_lshl_add_u32 v182, v8, 10, v3
	v_mov_b32_e32 v183, v1
	v_mov_b32_e32 v181, v1
	s_waitcnt vmcnt(1)
	v_lshl_add_u32 v0, v0, 10, v3
	s_waitcnt vmcnt(0)
	v_lshl_add_u32 v184, v4, 10, v3
	v_ashrrev_i32_e32 v3, 31, v2
	v_lshl_add_u64 v[2:3], v[2:3], 2, s[4:5]
	global_load_dword v4, v[2:3], off
	s_lshl_b32 s4, s15, 21
	global_load_dword v2, v[2:3], off offset:512
	s_add_u32 s50, s20, s4
	s_addc_u32 s51, s21, 0
	s_add_i32 s60, s14, 0
	s_add_i32 s61, s60, 0x10000
	s_mov_b32 m0, s61
	s_add_i32 s62, s60, 0x12000
	global_load_lds_dwordx4 v182, s[50:51]
	s_mov_b32 m0, s62
	s_add_i32 s63, s60, 0x2000
	global_load_lds_dwordx4 v180, s[50:51]
	s_mov_b32 m0, s60
	s_add_u32 s4, s50, 0x20000
	global_load_lds_dwordx4 v0, s[12:13]
	s_mov_b32 m0, s63
	s_addc_u32 s5, s51, 0
	s_add_i32 s64, s60, 0x14000
	s_add_i32 s65, s60, 0x16000
	s_add_i32 s66, s60, 0x4000
	s_add_i32 s67, s60, 0x6000
	s_cmp_lg_u32 s9, 1
	s_waitcnt vmcnt(0)
	v_lshl_add_u32 v196, v4, 10, v7
	global_load_lds_dwordx4 v196, s[12:13]
	s_mov_b32 m0, s64
	v_lshl_add_u32 v198, v2, 10, v7
	global_load_lds_dwordx4 v182, s[4:5]
	s_mov_b32 m0, s65
	v_lshl_add_u64 v[2:3], s[50:51], 0, v[182:183]
	global_load_lds_dwordx4 v180, s[4:5]
	s_mov_b32 m0, s66
	v_lshl_add_u64 v[4:5], s[50:51], 0, v[180:181]
	global_load_lds_dwordx4 v184, s[12:13]
	s_mov_b32 m0, s67
	s_nop 0
	global_load_lds_dwordx4 v198, s[12:13]
	s_cbranch_scc1 .LBB0_1688
	s_barrier

.LBB0_1690:
	s_add_i32 s79, s79, 1
	v_readlane_b32 s4, v252, 53
	s_mul_i32 s4, s79, s4
	s_mul_hi_u32 s5, s79, s2
	s_add_i32 s5, s5, s4
	s_mul_i32 s4, s79, s2
	s_add_u32 s8, s4, s88
	v_readlane_b32 s4, v252, 50
	s_addc_u32 s9, s5, s4
	v_cmp_ge_i64_e64 s[4:5], s[8:9], v[178:179]
	v_cmp_lt_i64_e64 s[6:7], s[8:9], v[178:179]
	s_and_b64 vcc, exec, s[4:5]
	s_cbranch_vccnz .LBB0_1702
	s_ashr_i32 s9, s8, 31
	s_lshr_b32 s9, s9, 29
	s_add_i32 s9, s8, s9
	s_ashr_i32 s40, s9, 3
	s_and_b32 s9, s9, -8
	s_sub_i32 s8, s8, s9
	s_lshr_b32 s9, s8, 31
	s_add_i32 s9, s27, s9
	s_mul_i32 s8, s9, s8
	s_add_i32 s8, s8, s40
	s_ashr_i32 s9, s8, 31
	s_lshr_b32 s9, s9, 27
	s_add_i32 s9, s8, s9
	s_ashr_i32 s40, s9, 5
	s_lshl_b32 s41, s40, 2
	s_sub_i32 s40, s27, s41
	s_min_i32 s42, s40, 4
	s_abs_i32 s40, s42
	v_cvt_f32_u32_e32 v2, s40
	s_sub_i32 s44, 0, s40
	s_andn2_b32 s9, s9, 31
	s_sub_i32 s8, s8, s9
	v_rcp_iflag_f32_e32 v2, v2
	s_abs_i32 s9, s8
	s_xor_b32 s43, s8, s42
	s_ashr_i32 s43, s43, 31
	v_mul_f32_e32 v2, 0x4f7ffffe, v2
	v_cvt_u32_f32_e32 v2, v2
	s_nop 0
	v_readfirstlane_b32 s45, v2
	s_mul_i32 s44, s44, s45
	s_mul_hi_u32 s44, s45, s44
	s_add_i32 s45, s45, s44
	s_mul_hi_u32 s44, s9, s45
	s_mul_i32 s45, s44, s40
	s_sub_i32 s9, s9, s45
	s_add_i32 s47, s44, 1
	s_sub_i32 s45, s9, s40
	s_cmp_ge_u32 s9, s40
	s_cselect_b32 s44, s47, s44
	s_cselect_b32 s9, s45, s9
	s_add_i32 s45, s44, 1
	s_cmp_ge_u32 s9, s40
	s_cselect_b32 s9, s45, s44
	s_xor_b32 s9, s9, s43
	s_sub_i32 s40, s9, s43
	s_mul_i32 s9, s40, s42
	s_sub_i32 s8, s8, s9
	s_add_i32 s42, s8, s41
	s_mov_b64 s[8:9], 0
	s_andn2_b64 vcc, exec, s[6:7]
	s_mov_b64 s[44:45], s[50:51]
	s_cbranch_vccz .LBB0_1703

.LBB0_1779:
	v_ashrrev_i32_e32 v3, 31, v0
	v_lshrrev_b32_e32 v3, 26, v3
	v_lshlrev_b32_e32 v2, 4, v0
	v_add_u32_e32 v3, v0, v3
	v_bfe_i32 v0, v0, 27, 1
	v_lshrrev_b32_e32 v0, 22, v0
	v_add_u32_e32 v0, v2, v0
	v_and_b32_e32 v0, 0xfffffc00, v0
	v_sub_u32_e32 v0, v2, v0
	v_ashrrev_i32_e32 v11, 6, v3
	v_lshrrev_b32_e32 v3, 4, v0
	v_bitop3_b32 v0, v3, v0, 32 bitop3:0x6c
	v_ashrrev_i32_e32 v4, 31, v0
	s_add_u32 s51, s6, 0x9a000000
	v_readlane_b32 s4, v255, 4
	v_lshrrev_b32_e32 v4, 26, v4
	s_addc_u32 s52, s7, 0
	v_readlane_b32 s5, v255, 5
	s_lshl_b32 s28, s4, 15
	v_add_u32_e32 v4, v0, v4
	s_lshl_b64 s[4:5], s[28:29], 10
	v_lshlrev_b32_e32 v3, 3, v11
	v_ashrrev_i32_e32 v12, 6, v4
	v_and_b32_e32 v4, 0xc0, v4
	s_add_u32 s4, s6, s4
	v_and_b32_e32 v3, -16, v3
	v_sub_u32_e32 v0, v0, v4
	s_addc_u32 s5, s7, s5
	v_add_u32_e32 v3, v12, v3
	v_ashrrev_i16_sdwa v0, v228, sext(v0) dst_sel:DWORD dst_unused:UNUSED_PAD src0_sel:DWORD src1_sel:BYTE_0
	s_add_u32 s53, s4, 0x24400000
	v_lshlrev_b32_e32 v5, 5, v11
	v_bfe_i32 v13, v0, 0, 16
	v_lshlrev_b32_e32 v0, 1, v3
	v_lshrrev_b32_e32 v4, 2, v3
	v_and_b32_e32 v6, 3, v12
	s_mov_b32 s4, 0x3fffe0
	v_and_b32_e32 v5, 32, v5
	v_and_b32_e32 v0, 24, v0
	v_and_b32_e32 v4, 4, v4
	v_and_or_b32 v6, v3, s4, v6
	v_or3_b32 v0, v6, v4, v0
	v_add_lshl_u32 v4, v5, v13, 1
	v_add_u32_e32 v2, 0x2000, v2
	v_lshl_add_u32 v146, v3, 10, v4
	v_ashrrev_i32_e32 v3, 31, v2
	v_lshrrev_b32_e32 v3, 22, v3
	v_add_u32_e32 v3, v2, v3
	v_ashrrev_i32_e32 v14, 10, v3
	v_mul_i32_i24_e32 v3, 0x400, v14
	v_sub_u32_e32 v2, v2, v3
	v_lshrrev_b32_e32 v3, 4, v2
	v_bitop3_b32 v2, v3, v2, 32 bitop3:0x6c
	v_lshl_add_u32 v0, v0, 10, v4
	v_ashrrev_i32_e32 v4, 31, v2
	v_lshrrev_b32_e32 v4, 26, v4
	v_lshlrev_b32_e32 v3, 3, v14
	v_add_u32_e32 v4, v2, v4
	v_and_b32_e32 v3, -16, v3
	v_ashrrev_i32_e32 v15, 6, v4
	v_add_u32_e32 v3, v15, v3
	v_and_b32_e32 v6, 3, v15
	v_and_or_b32 v6, v3, s4, v6
	v_readlane_b32 s4, v253, 30
	s_addc_u32 s54, s5, 0
	s_add_i32 s4, s14, s4
	s_ashr_i32 s5, s4, 31
	s_lshr_b32 s5, s5, 28
	v_and_b32_e32 v4, 0xc0, v4
	s_add_i32 s5, s4, s5
	v_sub_u32_e32 v2, v2, v4
	s_ashr_i32 s13, s5, 4
	v_ashrrev_i16_sdwa v2, v228, sext(v2) dst_sel:DWORD dst_unused:UNUSED_PAD src0_sel:DWORD src1_sel:BYTE_0
	s_lshl_b32 s14, s13, 2
	v_lshlrev_b32_e32 v5, 5, v14
	v_bfe_i32 v16, v2, 0, 16
	v_lshlrev_b32_e32 v2, 1, v3
	v_lshrrev_b32_e32 v4, 2, v3
	s_sub_i32 s13, s27, s14
	v_and_b32_e32 v5, 32, v5
	v_and_b32_e32 v2, 24, v2
	v_and_b32_e32 v4, 4, v4
	s_min_i32 s15, s13, 4
	v_or3_b32 v2, v6, v4, v2
	v_add_lshl_u32 v4, v5, v16, 1
	s_abs_i32 s20, s15
	v_lshl_add_u32 v148, v3, 10, v4
	v_cvt_f32_u32_e32 v3, s20
	v_lshl_add_u32 v150, v2, 10, v4
	s_sub_i32 s35, 0, s20
	s_andn2_b32 s5, s5, 15
	v_rcp_iflag_f32_e32 v2, v3
	s_sub_i32 s4, s4, s5
	s_abs_i32 s34, s4
	s_ashr_i32 s13, s46, 6
	v_mul_f32_e32 v2, 0x4f7ffffe, v2
	v_cvt_u32_f32_e32 v2, v2
	s_xor_b32 s5, s4, s15
	s_ashr_i32 s12, s46, 8
	s_lshl_b32 s21, s13, 10
	v_readfirstlane_b32 s38, v2
	s_mul_i32 s35, s35, s38
	s_mul_hi_u32 s35, s38, s35
	s_add_i32 s38, s38, s35
	s_mul_hi_u32 s35, s34, s38
	s_mul_i32 s38, s35, s20
	s_sub_i32 s34, s34, s38
	s_ashr_i32 s5, s5, 31
	s_add_i32 s38, s35, 1
	s_sub_i32 s39, s34, s20
	s_cmp_ge_u32 s34, s20
	s_cselect_b32 s35, s38, s35
	s_cselect_b32 s34, s39, s34
	s_add_i32 s38, s35, 1
	v_mbcnt_lo_u32_b32 v2, -1, 0
	v_mbcnt_hi_u32_b32 v2, -1, v2
	s_cmp_ge_u32 s34, s20
	v_and_b32_e32 v2, 31, v2
	s_cselect_b32 s20, s38, s35
	v_lshl_add_u32 v3, v2, 2, s31
	s_xor_b32 s20, s20, s5
	ds_read_b32 v3, v3 offset:4
	s_sub_i32 s40, s20, s5
	s_mul_i32 s5, s40, s15
	s_sub_i32 s4, s4, s5
	s_add_i32 s38, s14, s4
	v_cmp_ne_u32_e32 vcc, 31, v2
	s_waitcnt lgkmcnt(0)
	v_cmp_ge_i32_e64 s[4:5], s38, v3
	s_and_b64 s[4:5], vcc, s[4:5]
	s_ashr_i32 s39, s38, 31
	v_cndmask_b32_e64 v2, 0, 1, s[4:5]
	v_cmp_ne_u32_e32 vcc, 0, v2
	s_bcnt1_i32_b32 s20, vcc_lo
	s_ashr_i32 s41, s40, 31
	s_lshl_b64 s[14:15], s[38:39], 18
	s_lshl_b64 s[4:5], s[40:41], 18
	s_lshl_b32 s20, s20, 20
	s_add_u32 s4, s53, s4
	s_addc_u32 s5, s54, s5
	s_add_u32 s42, s4, s20
	s_addc_u32 s43, s5, 0
	s_add_i32 s55, s21, 0
	s_add_i32 s56, s55, 0x10000
	s_add_i32 s57, s55, 0x12000
	s_mov_b32 m0, s56
	s_add_u32 s44, s51, s14
	global_load_lds_dwordx4 v0, s[42:43]
	s_mov_b32 m0, s57
	s_addc_u32 s45, s52, s15
	s_add_i32 s58, s55, 0x2000
	global_load_lds_dwordx4 v150, s[42:43]
	s_mov_b32 m0, s55
	s_add_u32 s4, s42, 0x20000
	global_load_lds_dwordx4 v146, s[44:45]
	s_mov_b32 m0, s58
	s_addc_u32 s5, s43, 0
	s_add_i32 s59, s55, 0x14000
	global_load_lds_dwordx4 v148, s[44:45]
	s_mov_b32 m0, s59
	s_add_i32 s60, s55, 0x16000
	global_load_lds_dwordx4 v0, s[4:5]
	s_mov_b32 m0, s60
	v_mov_b32_e32 v151, v1
	global_load_lds_dwordx4 v150, s[4:5]
	s_add_u32 s4, s44, 0x20000
	s_addc_u32 s5, s45, 0
	s_add_i32 s61, s55, 0x4000
	s_mov_b32 m0, s61
	s_add_i32 s62, s55, 0x6000
	global_load_lds_dwordx4 v146, s[4:5]
	s_mov_b32 m0, s62
	v_mov_b32_e32 v147, v1
	global_load_lds_dwordx4 v148, s[4:5]
	v_mov_b32_e32 v149, v1
	v_lshl_add_u64 v[8:9], s[42:43], 0, v[0:1]
	v_lshl_add_u64 v[6:7], s[42:43], 0, v[150:151]
	v_lshl_add_u64 v[4:5], s[44:45], 0, v[146:147]
	s_cmp_lg_u32 s12, 1
	v_lshl_add_u64 v[2:3], s[44:45], 0, v[148:149]
	s_cbranch_scc1 .LBB0_1781
	s_barrier

.LBB0_1788:
	s_ashr_i32 s8, s14, 3
	s_add_i32 s8, s20, s8
	s_ashr_i32 s9, s8, 31
	s_lshr_b32 s9, s9, 28
	s_add_i32 s9, s8, s9
	s_ashr_i32 s14, s9, 4
	s_lshl_b32 s15, s14, 2
	s_sub_i32 s14, s27, s15
	s_min_i32 s20, s14, 4
	s_abs_i32 s14, s20
	v_cvt_f32_u32_e32 v2, s14
	s_sub_i32 s34, 0, s14
	s_andn2_b32 s9, s9, 15
	s_sub_i32 s8, s8, s9
	v_rcp_iflag_f32_e32 v2, v2
	s_abs_i32 s9, s8
	s_xor_b32 s21, s8, s20
	s_ashr_i32 s21, s21, 31
	v_mul_f32_e32 v2, 0x4f7ffffe, v2
	v_cvt_u32_f32_e32 v2, v2
	s_nop 0
	v_readfirstlane_b32 s35, v2
	s_mul_i32 s34, s34, s35
	s_mul_hi_u32 s34, s35, s34
	s_add_i32 s35, s35, s34
	s_mul_hi_u32 s34, s9, s35
	s_mul_i32 s35, s34, s14
	s_sub_i32 s9, s9, s35
	s_add_i32 s39, s34, 1
	s_sub_i32 s35, s9, s14
	s_cmp_ge_u32 s9, s14
	s_cselect_b32 s34, s39, s34
	s_cselect_b32 s9, s35, s9
	s_add_i32 s35, s34, 1
	s_cmp_ge_u32 s9, s14
	s_cselect_b32 s9, s35, s34
	s_xor_b32 s9, s9, s21
	s_sub_i32 s14, s9, s21
	s_mul_i32 s9, s14, s20
	s_sub_i32 s8, s8, s9
	s_add_i32 s20, s15, s8
